# mLSTM den: n vector stored XOR-swizzled in LDS so the per-part ds_read_b128 no longer conflict 4-way
# baseline (speedup 1.0000x reference)
.LBB0_732:
	ds_read_b128 v[92:95], v166
	v_add_u32_e32 v167, 0, v3
	v_add_u32_e32 v0, 0x10800, v167
	v_add_u32_e32 v3, 0x10a40, v167
	ds_read_b64_tr_b16 v[72:73], v0
	ds_read_b64_tr_b16 v[74:75], v3
	ds_read_b128 v[168:171], v166 offset:64
	v_add_u32_e32 v0, 0x11a00, v167
	v_add_u32_e32 v174, 0x11c40, v167
	ds_read_b32 v3, v124 offset:512
	ds_read_b64_tr_b16 v[172:173], v0
	ds_read_b64_tr_b16 v[174:175], v174
	ds_read_b128 v[176:179], v166 offset:2304
	ds_read_b128 v[180:183], v145
	s_waitcnt lgkmcnt(6)
	v_mfma_f32_16x16x32_bf16 v[92:95], v[92:95], v[72:75], 0
	s_waitcnt lgkmcnt(0)
	v_lshlrev_b32_e32 v0, 16, v180
	v_mfma_f32_16x16x32_bf16 v[92:95], v[168:171], v[172:175], v[92:95]
	v_lshlrev_b32_e32 v210, 2, v110
	v_and_b32_e32 v210, 0x60, v210
	v_add_u32_e32 v211, v146, v210
	v_xor_b32_e32 v212, 32, v210
	v_add_u32_e32 v212, v146, v212
	v_xor_b32_e32 v213, 64, v210
	v_add_u32_e32 v213, v146, v213
	v_xor_b32_e32 v214, 0x60, v210
	v_add_u32_e32 v214, v146, v214
	ds_read_b128 v[168:171], v145 offset:16
	ds_read_b128 v[184:187], v145 offset:32
	ds_read_b128 v[188:191], v145 offset:48
	ds_read_b128 v[194:197], v211
	ds_read_b128 v[198:201], v211 offset:16
	ds_read_b128 v[202:205], v212
	ds_read_b128 v[206:209], v212 offset:16
	v_and_b32_e32 v180, 0xffff0000, v180
	s_waitcnt lgkmcnt(3)
	v_mul_f32_e32 v180, v195, v180
	v_fmac_f32_e32 v180, v194, v0
	v_lshlrev_b32_e32 v0, 16, v181
	v_and_b32_e32 v181, 0xffff0000, v181
	v_mul_f32_e32 v181, v197, v181
	v_fmac_f32_e32 v181, v196, v0
	v_add_f32_e32 v0, v180, v181
	v_and_b32_e32 v181, 0xffff0000, v182
	v_lshlrev_b32_e32 v180, 16, v182
	s_waitcnt lgkmcnt(2)
	v_mul_f32_e32 v181, v199, v181
	v_fmac_f32_e32 v181, v198, v180
	v_add_f32_e32 v0, v181, v0
	v_and_b32_e32 v181, 0xffff0000, v183
	v_lshlrev_b32_e32 v180, 16, v183
	v_mul_f32_e32 v181, v201, v181
	v_fmac_f32_e32 v181, v200, v180
	v_lshlrev_b32_e32 v180, 16, v168
	v_and_b32_e32 v168, 0xffff0000, v168
	s_waitcnt lgkmcnt(1)
	v_mul_f32_e32 v168, v203, v168
	v_fmac_f32_e32 v168, v202, v180
	v_lshlrev_b32_e32 v180, 16, v169
	v_and_b32_e32 v169, 0xffff0000, v169
	v_mul_f32_e32 v169, v205, v169
	v_fmac_f32_e32 v169, v204, v180
	v_add_f32_e32 v168, v168, v169
	v_lshlrev_b32_e32 v169, 16, v170
	v_and_b32_e32 v170, 0xffff0000, v170
	s_waitcnt lgkmcnt(0)
	v_mul_f32_e32 v170, v207, v170
	v_fmac_f32_e32 v170, v206, v169
	v_add_f32_e32 v168, v170, v168
	v_and_b32_e32 v170, 0xffff0000, v171
	v_lshlrev_b32_e32 v169, 16, v171
	v_mul_f32_e32 v170, v209, v170
	v_fmac_f32_e32 v170, v208, v169
	v_add_f32_e32 v180, v170, v168
	ds_read_b128 v[168:171], v213
	v_add_f32_e32 v0, v181, v0
	v_add_f32_e32 v0, 0, v0
	v_add_f32_e32 v0, v0, v180
	ds_read_b128 v[180:183], v213 offset:16
	v_lshlrev_b32_e32 v194, 16, v184
	v_and_b32_e32 v184, 0xffff0000, v184
	s_waitcnt lgkmcnt(1)
	v_mul_f32_e32 v169, v169, v184
	v_and_b32_e32 v184, 0xffff0000, v185
	v_fmac_f32_e32 v169, v168, v194
	v_lshlrev_b32_e32 v168, 16, v185
	v_mul_f32_e32 v171, v171, v184
	v_fmac_f32_e32 v171, v170, v168
	v_and_b32_e32 v170, 0xffff0000, v186
	v_add_f32_e32 v168, v169, v171
	v_lshlrev_b32_e32 v169, 16, v186
	s_waitcnt lgkmcnt(0)
	v_mul_f32_e32 v170, v181, v170
	v_fmac_f32_e32 v170, v180, v169
	v_add_f32_e32 v168, v170, v168
	v_and_b32_e32 v170, 0xffff0000, v187
	v_lshlrev_b32_e32 v169, 16, v187
	v_mul_f32_e32 v170, v183, v170
	v_fmac_f32_e32 v170, v182, v169
	v_add_f32_e32 v180, v170, v168
	ds_read_b128 v[168:171], v214
	v_add_f32_e32 v0, v0, v180
	ds_read_b128 v[180:183], v214 offset:16
	v_and_b32_e32 v185, 0xffff0000, v188
	v_lshlrev_b32_e32 v184, 16, v188
	s_waitcnt lgkmcnt(1)
	v_mul_f32_e32 v169, v169, v185
	v_fmac_f32_e32 v169, v168, v184
	v_and_b32_e32 v184, 0xffff0000, v189
	v_lshlrev_b32_e32 v168, 16, v189
	v_mul_f32_e32 v171, v171, v184
	v_fmac_f32_e32 v171, v170, v168
	v_and_b32_e32 v170, 0xffff0000, v190
	v_add_f32_e32 v168, v169, v171
	v_lshlrev_b32_e32 v169, 16, v190
	s_waitcnt lgkmcnt(0)
	v_mul_f32_e32 v170, v181, v170
	v_fmac_f32_e32 v170, v180, v169
	v_add_f32_e32 v180, v170, v168
	ds_read_b128 v[168:171], v147
	v_and_b32_e32 v184, 0xffff0000, v191
	v_lshlrev_b32_e32 v181, 16, v191
	v_mul_f32_e32 v183, v183, v184
	v_fmac_f32_e32 v183, v182, v181
	v_add_f32_e32 v180, v183, v180
	v_add_f32_e32 v0, v0, v180
	s_waitcnt lgkmcnt(0)
	v_lshlrev_b32_e32 v180, 16, v168
	v_and_b32_e32 v168, 0xffff0000, v168
	v_add_f32_e32 v168, v180, v168
	v_lshlrev_b32_e32 v180, 16, v169
	v_and_b32_e32 v169, 0xffff0000, v169
	v_add_f32_e32 v169, v180, v169
	v_add_f32_e32 v168, v168, v169
	v_lshlrev_b32_e32 v169, 16, v170
	v_and_b32_e32 v170, 0xffff0000, v170
	v_add_f32_e32 v169, v169, v170
	v_add_f32_e32 v168, v169, v168
	v_lshlrev_b32_e32 v169, 16, v171
	v_and_b32_e32 v170, 0xffff0000, v171
	v_add_f32_e32 v169, v169, v170
	v_add_f32_e32 v180, v169, v168
	v_fmac_f32_e32 v180, v3, v0
	ds_read_b128 v[168:171], v166 offset:2368
	v_mfma_f32_16x16x32_bf16 v[72:75], v[176:179], v[72:75], 0
	s_nop 0
	v_add_f32_dpp v0, v180, v180 quad_perm:[1,0,3,2] row_mask:0xf bank_mask:0xf
	s_nop 1
	v_add_f32_dpp v3, v0, v0 quad_perm:[2,3,0,1] row_mask:0xf bank_mask:0xf
	s_nop 1
	v_add_f32_dpp v0, v3, v3 row_half_mirror row_mask:0xf bank_mask:0xf
	s_waitcnt lgkmcnt(0)
	v_mfma_f32_16x16x32_bf16 v[72:75], v[168:171], v[172:175], v[72:75]
	s_and_saveexec_b64 s[80:81], s[58:59]
	s_cbranch_execz .LBB0_734
	ds_write_b32 v124, v0 offset:1280
.LBB0_734:
	s_or_b64 exec, exec, s[80:81]
	v_cndmask_b32_e64 v171, v79, v87, s[62:63]
	v_cndmask_b32_e64 v170, v78, v86, s[62:63]
	v_cndmask_b32_e64 v169, v77, v85, s[62:63]
	v_cndmask_b32_e64 v168, v76, v84, s[62:63]
	v_cndmask_b32_e64 v172, v80, v88, s[62:63]
	v_add_u32_e32 v0, s11, v131
	v_cndmask_b32_e64 v175, v83, v91, s[62:63]
	v_cndmask_b32_e64 v174, v82, v90, s[62:63]
	v_cndmask_b32_e64 v173, v81, v89, s[62:63]
	ds_write_b128 v0, v[168:171]
	ds_write_b128 v0, v[172:175] offset:1024
	v_cndmask_b32_e64 v172, v84, v76, s[62:63]
	v_add_u32_e32 v76, s21, v131
	s_waitcnt lgkmcnt(0)
	s_barrier
	v_cndmask_b32_e64 v0, v87, v79, s[62:63]
	v_cndmask_b32_e64 v3, v86, v78, s[62:63]
	v_cndmask_b32_e64 v178, v85, v77, s[62:63]
	v_cndmask_b32_e64 v179, v91, v83, s[62:63]
	v_cndmask_b32_e64 v180, v90, v82, s[62:63]
	v_cndmask_b32_e64 v181, v89, v81, s[62:63]
	v_cndmask_b32_e64 v182, v88, v80, s[62:63]
	ds_read_b128 v[80:83], v76
	ds_read_b128 v[76:79], v76 offset:1024
	ds_read_b128 v[84:87], v159
	ds_read_b128 v[88:91], v160
	ds_read_b128 v[168:171], v161
	s_waitcnt lgkmcnt(4)
	v_add_f32_e32 v80, v172, v80
	v_lshl_add_u64 v[174:175], v[104:105], 0, s[88:89]
	s_waitcnt lgkmcnt(2)
	v_fma_f32 v80, v80, v84, v92
	s_waitcnt lgkmcnt(1)
	v_max_f32_e64 v88, |v88|, |v88|
	s_waitcnt lgkmcnt(0)
	v_max_f32_e32 v84, v168, v168
	v_max_f32_e32 v84, v88, v84
	v_div_scale_f32 v88, s[80:81], v84, v84, v80
	v_rcp_f32_e32 v92, v88
	s_mov_b32 s80, 0x3a800000
	v_add_f32_e32 v3, v3, v82
	v_fma_f32 v3, v3, v86, v94
	v_fma_f32 v168, -v88, v92, 1.0
	v_fmac_f32_e32 v92, v168, v92
	v_div_scale_f32 v168, vcc, v80, v84, v80
	v_mul_f32_e32 v172, v168, v92
	v_fma_f32 v173, -v88, v172, v168
	v_fmac_f32_e32 v172, v173, v92
	v_fma_f32 v88, -v88, v172, v168
	v_div_fmas_f32 v88, v88, v92, v172
	v_div_fixup_f32 v80, v88, v84, v80
	v_add_co_u32_e32 v176, vcc, s80, v174
	v_cvt_pk_bf16_f32 v80, v80, v1
	v_max_f32_e64 v84, |v89|, |v89|
	s_nop 0
	v_addc_co_u32_e32 v177, vcc, 0, v175, vcc
	global_store_short v[176:177], v80, off
	v_add_f32_e32 v80, v178, v81
	v_max_f32_e32 v81, v169, v169
	v_fma_f32 v80, v80, v85, v93
	v_max_f32_e32 v81, v84, v81
	v_div_scale_f32 v84, s[80:81], v81, v81, v80
	v_rcp_f32_e32 v85, v84
	v_lshl_add_u64 v[172:173], v[106:107], 0, s[88:89]
	v_add_f32_e32 v0, v0, v83
	v_fmac_f32_e32 v95, v0, v87
	v_fma_f32 v88, -v84, v85, 1.0
	v_fmac_f32_e32 v85, v88, v85
	v_div_scale_f32 v88, vcc, v80, v81, v80
	v_mul_f32_e32 v89, v88, v85
	v_fma_f32 v92, -v84, v89, v88
	v_fmac_f32_e32 v89, v92, v85
	v_fma_f32 v84, -v84, v89, v88
	v_div_fmas_f32 v84, v84, v85, v89
	v_div_fixup_f32 v80, v84, v81, v80
	v_cvt_pk_bf16_f32 v84, v80, v1
	v_or_b32_e32 v80, 0x800, v172
	v_mov_b32_e32 v81, v173
	v_lshl_add_u64 v[80:81], v[102:103], 0, v[80:81]
	global_store_short v[80:81], v84, off
	v_max_f32_e32 v80, v170, v170
	v_max_f32_e64 v81, |v90|, |v90|
	v_max_f32_e32 v80, v81, v80
	v_div_scale_f32 v81, s[80:81], v80, v80, v3
	v_rcp_f32_e32 v82, v81
	v_max_f32_e32 v0, v171, v171
	v_lshl_add_u64 v[92:93], v[172:173], 0, s[96:97]
	v_fma_f32 v84, -v81, v82, 1.0
	v_fmac_f32_e32 v82, v84, v82
	v_div_scale_f32 v84, vcc, v3, v80, v3
	v_mul_f32_e32 v85, v84, v82
	v_fma_f32 v86, -v81, v85, v84
	v_fmac_f32_e32 v85, v86, v82
	v_fma_f32 v81, -v81, v85, v84
	v_div_fmas_f32 v81, v81, v82, v85
	v_div_fixup_f32 v3, v81, v80, v3
	v_or_b32_e32 v80, 0x1000, v172
	v_mov_b32_e32 v81, v173
	v_cvt_pk_bf16_f32 v3, v3, v1
	v_lshl_add_u64 v[80:81], v[102:103], 0, v[80:81]
	global_store_short v[80:81], v3, off
	v_max_f32_e64 v3, |v91|, |v91|
	v_max_f32_e32 v0, v3, v0
	v_div_scale_f32 v3, s[80:81], v0, v0, v95
	v_rcp_f32_e32 v80, v3
	s_nop 0
	v_fma_f32 v81, -v3, v80, 1.0
	v_fmac_f32_e32 v80, v81, v80
	v_div_scale_f32 v81, vcc, v95, v0, v95
	v_mul_f32_e32 v82, v81, v80
	v_fma_f32 v83, -v3, v82, v81
	v_fmac_f32_e32 v82, v83, v80
	v_fma_f32 v3, -v3, v82, v81
	v_div_fmas_f32 v3, v3, v80, v82
	v_or_b32_e32 v80, 0x1800, v172
	v_mov_b32_e32 v81, v173
	v_div_fixup_f32 v0, v3, v0, v95
	v_lshl_add_u64 v[80:81], v[102:103], 0, v[80:81]
	v_cvt_pk_bf16_f32 v0, v0, v1
	global_store_short v[80:81], v0, off
	ds_read_b128 v[80:83], v159 offset:64
	ds_read_b128 v[84:87], v160 offset:64
	ds_read_b128 v[88:91], v161 offset:64
	v_add_f32_e32 v0, v182, v76
	s_waitcnt lgkmcnt(0)
	v_fma_f32 v0, v0, v80, v72
	v_max_f32_e64 v72, |v84|, |v84|
	v_max_f32_e32 v3, v88, v88
	v_max_f32_e32 v3, v72, v3
	v_div_scale_f32 v72, s[80:81], v3, v3, v0
	v_rcp_f32_e32 v76, v72
	s_mov_b32 s80, 0x3a808000
	v_fma_f32 v80, -v72, v76, 1.0
	v_fmac_f32_e32 v76, v80, v76
	v_div_scale_f32 v80, vcc, v0, v3, v0
	v_mul_f32_e32 v84, v80, v76
	v_fma_f32 v88, -v72, v84, v80
	v_fmac_f32_e32 v84, v88, v76
	v_fma_f32 v72, -v72, v84, v80
	v_div_fmas_f32 v72, v72, v76, v84
	v_div_fixup_f32 v0, v72, v3, v0
	v_add_co_u32_e32 v94, vcc, s80, v174
	v_cvt_pk_bf16_f32 v0, v0, v1
	v_max_f32_e32 v3, v89, v89
	s_nop 0
	v_addc_co_u32_e32 v95, vcc, 0, v175, vcc
	global_store_short v[94:95], v0, off
	v_add_f32_e32 v0, v181, v77
	v_max_f32_e64 v72, |v85|, |v85|
	v_fma_f32 v0, v0, v81, v73
	v_max_f32_e32 v3, v72, v3
	v_div_scale_f32 v72, s[80:81], v3, v3, v0
	v_rcp_f32_e32 v73, v72
	v_add_u32_e32 v94, 0, v2
	v_fma_f32 v76, -v72, v73, 1.0
	v_fmac_f32_e32 v73, v76, v73
	v_div_scale_f32 v76, vcc, v0, v3, v0
	v_mul_f32_e32 v77, v76, v73
	v_fma_f32 v80, -v72, v77, v76
	v_fmac_f32_e32 v77, v80, v73
	v_fma_f32 v72, -v72, v77, v76
	v_div_fmas_f32 v72, v72, v73, v77
	v_div_fixup_f32 v0, v72, v3, v0
	v_or_b32_e32 v72, 0x800, v92
	v_mov_b32_e32 v73, v93
	v_cvt_pk_bf16_f32 v0, v0, v1
	v_lshl_add_u64 v[72:73], v[102:103], 0, v[72:73]
	global_store_short v[72:73], v0, off
	v_add_f32_e32 v0, v180, v78
	v_max_f32_e32 v3, v90, v90
	v_max_f32_e64 v72, |v86|, |v86|
	v_fma_f32 v0, v0, v82, v74
	v_max_f32_e32 v3, v72, v3
	v_div_scale_f32 v72, s[80:81], v3, v3, v0
	v_rcp_f32_e32 v73, v72
	s_nop 0
	v_fma_f32 v74, -v72, v73, 1.0
	v_fmac_f32_e32 v73, v74, v73
	v_div_scale_f32 v74, vcc, v0, v3, v0
	v_mul_f32_e32 v76, v74, v73
	v_fma_f32 v77, -v72, v76, v74
	v_fmac_f32_e32 v76, v77, v73
	v_fma_f32 v72, -v72, v76, v74
	v_div_fmas_f32 v72, v72, v73, v76
	v_div_fixup_f32 v0, v72, v3, v0
	v_or_b32_e32 v72, 0x1000, v92
	v_mov_b32_e32 v73, v93
	v_cvt_pk_bf16_f32 v0, v0, v1
	v_lshl_add_u64 v[72:73], v[102:103], 0, v[72:73]
	global_store_short v[72:73], v0, off
	v_add_f32_e32 v0, v179, v79
	v_fmac_f32_e32 v75, v0, v83
	v_max_f32_e32 v0, v91, v91
	v_max_f32_e64 v3, |v87|, |v87|
	v_max_f32_e32 v0, v3, v0
	v_div_scale_f32 v3, s[80:81], v0, v0, v75
	v_rcp_f32_e32 v72, v3
	v_or_b32_e32 v92, 0x1800, v92
	v_fma_f32 v73, -v3, v72, 1.0
	v_fmac_f32_e32 v72, v73, v72
	v_div_scale_f32 v73, vcc, v75, v0, v75
	v_mul_f32_e32 v74, v73, v72
	v_fma_f32 v76, -v3, v74, v73
	v_fmac_f32_e32 v74, v76, v72
	v_fma_f32 v3, -v3, v74, v73
	v_div_fmas_f32 v3, v3, v72, v74
	v_div_fixup_f32 v0, v3, v0, v75
	v_cvt_pk_bf16_f32 v0, v0, v1
	v_lshl_add_u64 v[72:73], v[102:103], 0, v[92:93]
	global_store_short v[72:73], v0, off
	v_mov_b32_e32 v0, s19
	ds_read_b32 v92, v0
	v_add_u32_e32 v0, 0x12c00, v167
	v_add_u32_e32 v3, 0x12e40, v167
	ds_read_b64_tr_b16 v[80:81], v0
	ds_read_b64_tr_b16 v[82:83], v3
	ds_read_b128 v[72:75], v135
	ds_read_b128 v[76:79], v135 offset:16
	v_add_u32_e32 v0, 0x13e00, v167
	v_add_u32_e32 v3, 0x14040, v167
	ds_read_b64_tr_b16 v[206:207], v0
	ds_read_b64_tr_b16 v[208:209], v3
	ds_read_b128 v[198:201], v135 offset:128
	ds_read_b128 v[202:205], v135 offset:144
	s_mov_b32 s98, 0
	s_and_b64 vcc, exec, s[28:29]
	s_cselect_b32 s98, 64, s98
	s_and_b64 vcc, exec, s[30:31]
	s_cselect_b32 s98, 0x80, s98
	s_and_b64 vcc, exec, s[34:35]
	s_cselect_b32 s98, 0xc0, s98
	v_add_u32_e32 v88, s98, v94
	ds_read_b64_tr_b16 v[168:169], v94
	ds_read_b64_tr_b16 v[170:171], v94 offset:2112
	ds_read_b64_tr_b16 v[172:173], v94 offset:32
	ds_read_b64_tr_b16 v[174:175], v94 offset:2144
	ds_read_b64_tr_b16 v[176:177], v94 offset:64
	ds_read_b64_tr_b16 v[178:179], v94 offset:2176
	s_waitcnt lgkmcnt(6)
	v_cvt_pk_bf16_f32 v84, v72, v73
	v_cvt_pk_bf16_f32 v85, v74, v75
	v_cvt_pk_bf16_f32 v86, v76, v77
	v_cvt_pk_bf16_f32 v87, v78, v79
	v_cvt_pk_bf16_f32 v194, v198, v199
	v_cvt_pk_bf16_f32 v195, v200, v201
	v_cvt_pk_bf16_f32 v196, v202, v203
	v_cvt_pk_bf16_f32 v197, v204, v205
	v_mov_b32_e32 v93, v92
	v_pk_mul_f32 v[68:69], v[68:69], v[92:93]
	v_pk_mul_f32 v[70:71], v[70:71], v[92:93]
	v_pk_mul_f32 v[64:65], v[64:65], v[92:93]
	v_pk_mul_f32 v[66:67], v[66:67], v[92:93]
	v_pk_mul_f32 v[56:57], v[56:57], v[92:93]
	v_pk_mul_f32 v[58:59], v[58:59], v[92:93]
	v_pk_mul_f32 v[60:61], v[60:61], v[92:93]
	v_pk_mul_f32 v[62:63], v[62:63], v[92:93]
	v_pk_mul_f32 v[48:49], v[48:49], v[92:93]
	v_pk_mul_f32 v[50:51], v[50:51], v[92:93]
	v_pk_mul_f32 v[52:53], v[52:53], v[92:93]
	v_pk_mul_f32 v[54:55], v[54:55], v[92:93]
	v_pk_mul_f32 v[40:41], v[40:41], v[92:93]
	v_pk_mul_f32 v[42:43], v[42:43], v[92:93]
	v_pk_mul_f32 v[44:45], v[44:45], v[92:93]
	v_pk_mul_f32 v[46:47], v[46:47], v[92:93]
	ds_read_b64_tr_b16 v[180:181], v94 offset:96
	ds_read_b64_tr_b16 v[182:183], v94 offset:2208
	ds_read_b64_tr_b16 v[184:185], v94 offset:128
	ds_read_b64_tr_b16 v[186:187], v94 offset:2240
	ds_read_b64_tr_b16 v[188:189], v94 offset:160
	ds_read_b64_tr_b16 v[190:191], v94 offset:2272
	s_waitcnt lgkmcnt(10)
	v_mfma_f32_16x16x32_bf16 v[68:71], v[168:171], v[80:83], v[68:71]
	ds_read_b64_tr_b16 v[168:169], v94 offset:192
	ds_read_b64_tr_b16 v[170:171], v94 offset:2304
	s_waitcnt lgkmcnt(10)
	v_mfma_f32_16x16x32_bf16 v[64:67], v[172:175], v[80:83], v[64:67]
	ds_read_b64_tr_b16 v[172:173], v94 offset:224
	ds_read_b64_tr_b16 v[174:175], v94 offset:2336
	s_waitcnt lgkmcnt(10)
	v_mfma_f32_16x16x32_bf16 v[56:59], v[176:179], v[80:83], v[56:59]
	ds_read_b64_tr_b16 v[176:177], v88
	ds_read_b64_tr_b16 v[178:179], v88 offset:2112
	s_waitcnt lgkmcnt(10)
	v_mfma_f32_16x16x32_bf16 v[60:63], v[180:183], v[80:83], v[60:63]
	ds_read_b64_tr_b16 v[180:181], v88 offset:32
	ds_read_b64_tr_b16 v[182:183], v88 offset:2144
	s_waitcnt lgkmcnt(10)
	v_mfma_f32_16x16x32_bf16 v[48:51], v[184:187], v[80:83], v[48:51]
	ds_read_b64_tr_b16 v[184:185], v94 offset:16896
	ds_read_b64_tr_b16 v[186:187], v94 offset:19008
	s_waitcnt lgkmcnt(10)
	v_mfma_f32_16x16x32_bf16 v[52:55], v[188:191], v[80:83], v[52:55]
	ds_read_b64_tr_b16 v[188:189], v94 offset:16928
	ds_read_b64_tr_b16 v[190:191], v94 offset:19040
	s_waitcnt lgkmcnt(10)
	v_mfma_f32_16x16x32_bf16 v[40:43], v[168:171], v[80:83], v[40:43]
	ds_read_b64_tr_b16 v[168:169], v94 offset:16960
	ds_read_b64_tr_b16 v[170:171], v94 offset:19072
	s_waitcnt lgkmcnt(10)
	v_mfma_f32_16x16x32_bf16 v[44:47], v[172:175], v[80:83], v[44:47]
	ds_read_b64_tr_b16 v[172:173], v94 offset:16992
	ds_read_b64_tr_b16 v[174:175], v94 offset:19104
	s_waitcnt lgkmcnt(10)
	v_mfma_f32_16x16x32_bf16 v[72:75], v[176:179], v[84:87], 0
	ds_read_b64_tr_b16 v[176:177], v94 offset:17024
	ds_read_b64_tr_b16 v[178:179], v94 offset:19136
	s_waitcnt lgkmcnt(10)
	v_mfma_f32_16x16x32_bf16 v[76:79], v[180:183], v[84:87], 0
	ds_read_b64_tr_b16 v[180:181], v94 offset:17056
	ds_read_b64_tr_b16 v[182:183], v94 offset:19168
	s_waitcnt lgkmcnt(10)
	v_mfma_f32_16x16x32_bf16 v[68:71], v[184:187], v[206:209], v[68:71]
	ds_read_b64_tr_b16 v[184:185], v94 offset:17088
	ds_read_b64_tr_b16 v[186:187], v94 offset:19200
	s_waitcnt lgkmcnt(10)
	v_mfma_f32_16x16x32_bf16 v[64:67], v[188:191], v[206:209], v[64:67]
	ds_read_b64_tr_b16 v[188:189], v94 offset:17120
	ds_read_b64_tr_b16 v[190:191], v94 offset:19232
	s_waitcnt lgkmcnt(10)
	v_mfma_f32_16x16x32_bf16 v[56:59], v[168:171], v[206:209], v[56:59]
	ds_read_b64_tr_b16 v[168:169], v88 offset:16896
	ds_read_b64_tr_b16 v[170:171], v88 offset:19008
	s_waitcnt lgkmcnt(10)
	v_mfma_f32_16x16x32_bf16 v[60:63], v[172:175], v[206:209], v[60:63]
	ds_read_b64_tr_b16 v[172:173], v88 offset:16928
	ds_read_b64_tr_b16 v[174:175], v88 offset:19040
	s_waitcnt lgkmcnt(10)
	v_mfma_f32_16x16x32_bf16 v[48:51], v[176:179], v[206:209], v[48:51]
	s_waitcnt lgkmcnt(8)
	v_mfma_f32_16x16x32_bf16 v[52:55], v[180:183], v[206:209], v[52:55]
	s_waitcnt lgkmcnt(6)
	v_mfma_f32_16x16x32_bf16 v[40:43], v[184:187], v[206:209], v[40:43]
	s_waitcnt lgkmcnt(4)
	v_mfma_f32_16x16x32_bf16 v[44:47], v[188:191], v[206:209], v[44:47]
	s_waitcnt lgkmcnt(2)
	v_mfma_f32_16x16x32_bf16 v[72:75], v[168:171], v[194:197], v[72:75]
	s_waitcnt lgkmcnt(0)
	v_mfma_f32_16x16x32_bf16 v[76:79], v[172:175], v[194:197], v[76:79]
	s_mov_b32 s99, 64
	s_and_b64 vcc, exec, s[62:63]
	s_cselect_b32 s99, 0, s99
	s_or_b64 vcc, s[30:31], s[34:35]
	s_and_b64 vcc, exec, vcc
	s_cselect_b32 s98, 32, 0
	s_or_b32 s99, s99, s98
	s_and_saveexec_b64 s[80:81], s[60:61]
	s_cbranch_execz .LBB0_725
	v_xor_b32_e32 v88, s99, v154
	v_add_u32_e32 v89, 64, v154
	v_xor_b32_e32 v89, s99, v89
	ds_read_b128 v[80:83], v88
	ds_read_b128 v[84:87], v89
	s_nop 7
	s_waitcnt lgkmcnt(1)
	v_pk_fma_f32 v[74:75], v[92:93], v[82:83], v[74:75]
	v_pk_fma_f32 v[72:73], v[92:93], v[80:81], v[72:73]
	s_waitcnt lgkmcnt(0)
	v_pk_fma_f32 v[78:79], v[92:93], v[86:87], v[78:79]
	v_pk_fma_f32 v[76:77], v[92:93], v[84:85], v[76:77]
	ds_write_b128 v88, v[72:75]
	ds_write_b128 v89, v[76:79]
	s_branch .LBB0_725
